# g2p with the MLA static priority raise on waves 0-3 instead of 4-7 (per-half A/B of the priority lever)
# baseline (speedup 1.0000x reference)
; #define LAS __attribute__((address_space(3)))
; __device__ __forceinline__ void mla_attn_phase(LAS unsigned char* lds, const bf16* Q, const bf16* KV, const bf16* Z, bf16* Oabc, const float* ropec, const float* ropes, int vcu, int G, int tid) {
;     using namespace fa;
;     asm volatile("" : "+v"(tid));
;     const int wid = __builtin_amdgcn_readfirstlane(tid >> 6), lane = tid & 63, r32 = lane & 31, hi = lane >> 5;
;     constexpr int SHM_K = 64 * 384, SHM_V = 16384;
;     LAS unsigned char* K_lds = lds; LAS unsigned char* V_lds = lds + 2 * SHM_K;
;     LAS float* wsf = (LAS float*)(lds + 2 * SHM_K + 2 * SHM_V) + wid * 64; LAS float* li_l = wsf; LAS float* al_l = wsf + 32;
.LBB0_1119:
	v_readlane_b32 s12, v252, 6
	v_readlane_b32 s8, v252, 4
	v_readlane_b32 s18, v252, 12
	v_readlane_b32 s19, v252, 13
	v_readlane_b32 s9, v252, 5
	s_mov_b64 s[6:7], s[18:19]
	v_mbcnt_lo_u32_b32 v0, -1, 0
	v_mbcnt_hi_u32_b32 v0, -1, v0
	v_readlane_b32 s0, v252, 37
	s_nop 3
	s_cmpk_lt_u32 s0, 0x100
	s_cbranch_scc0 .Lmla_prio_done
	s_setprio 1
